# baseline (speedup 1.0000x reference)
.LBB0_36:
	v_mfma_f32_32x32x16_bf16 v[112:127], a[192:195], a[128:131], v[0:15]
	v_mov_b32_e32 v200, v225
	v_mov_b32_e32 v201, v226
	s_nop 0
	v_permlane32_swap_b32_e32 v225, v200
	v_permlane32_swap_b32_e32 v226, v201
	v_add_f32_e32 v225, v225, v200
	v_add_f32_e32 v226, v226, v201
	v_mfma_f32_32x32x16_bf16 v[96:111], a[192:195], a[160:163], v[16:31]
	s_lshl_b32 s53, s50, 6
	s_add_i32 s53, s53, s52
	v_mov_b32_e32 v200, s53
	s_lshl_b32 s53, s50, 14
	s_add_i32 s53, s53, 0x10000
	v_mov_b32_e32 v201, s53
	v_mbcnt_lo_u32_b32 v204, -1, 0
	v_mbcnt_hi_u32_b32 v204, -1, v204
	v_mfma_f32_32x32x16_bf16 v[80:95], a[224:227], a[128:131], v[0:15]
	v_lshrrev_b32_e32 v202, 4, v204
	v_add_u32_e32 v203, 4, v202
	v_add_u32_e32 v205, 8, v202
	v_add_u32_e32 v206, 12, v202
	v_add_u32_e32 v207, 16, v202
	v_add_u32_e32 v208, 20, v202
	v_mfma_f32_32x32x16_bf16 v[64:79], a[224:227], a[160:163], v[16:31]
	v_add_u32_e32 v209, 24, v202
	v_add_u32_e32 v210, 28, v202
	v_exp_f32_e32 v48, v48
	v_exp_f32_e32 v49, v49
	v_mfma_f32_32x32x16_bf16 v[112:127], a[196:199], a[132:135], v[112:127]
	ds_read_b64_tr_b16 v[180:181], v215 offset:0
	v_cvt_pk_bf16_f32 v164, v128, v129
	v_exp_f32_e32 v50, v50
	v_exp_f32_e32 v51, v51
	v_mfma_f32_32x32x16_bf16 v[96:111], a[196:199], a[164:167], v[96:111]
	ds_read_b64_tr_b16 v[182:183], v215 offset:0x800
	v_cvt_pk_bf16_f32 v165, v130, v131
	v_exp_f32_e32 v218, v52
	v_exp_f32_e32 v219, v53
	v_mfma_f32_32x32x16_bf16 v[80:95], a[228:231], a[132:135], v[80:95]
	ds_read_b64_tr_b16 v[188:189], v215 offset:0x200
	v_cvt_pk_bf16_f32 v166, v132, v133
	ds_read_b64_tr_b16 v[190:191], v215 offset:0xa00
	ds_read_b64_tr_b16 v[176:177], v215 offset:0x400
	v_exp_f32_e32 v230, v54
	v_mfma_f32_32x32x16_bf16 v[64:79], a[228:231], a[164:167], v[64:79]
	v_exp_f32_e32 v231, v55
	v_cvt_pk_bf16_f32 v167, v134, v135
	v_exp_f32_e32 v220, v56
	v_exp_f32_e32 v221, v57
	v_mfma_f32_32x32x16_bf16 v[112:127], a[200:203], a[136:139], v[112:127]
	ds_read_b64_tr_b16 v[178:179], v215 offset:0xc00
	v_cvt_pk_bf16_f32 v128, v136, v137
	v_exp_f32_e32 v222, v58
	v_exp_f32_e32 v223, v59
	v_mfma_f32_32x32x16_bf16 v[96:111], a[200:203], a[168:171], v[96:111]
	ds_read_b64_tr_b16 v[184:185], v215 offset:0x600
	v_cvt_pk_bf16_f32 v129, v138, v139
	v_exp_f32_e32 v224, v60
	v_exp_f32_e32 v227, v61
	v_mfma_f32_32x32x16_bf16 v[80:95], a[232:235], a[136:139], v[80:95]
	ds_read_b64_tr_b16 v[186:187], v215 offset:0xe00
	v_cvt_pk_bf16_f32 v130, v140, v141
	ds_read_b64_tr_b16 v[172:173], v215 offset:0x1000
	v_exp_f32_e32 v228, v62
	v_exp_f32_e32 v229, v63
	v_mfma_f32_32x32x16_bf16 v[64:79], a[232:235], a[168:171], v[64:79]
	ds_read_b64_tr_b16 v[174:175], v215 offset:0x1800
	v_cvt_pk_bf16_f32 v131, v142, v143
	v_exp_f32_e32 v141, v32
	v_exp_f32_e32 v142, v33
	v_mfma_f32_32x32x16_bf16 v[112:127], a[204:207], a[140:143], v[112:127]
	ds_read_b64_tr_b16 v[168:169], v215 offset:0x1200
	v_cvt_pk_bf16_f32 v192, v144, v145
	v_exp_f32_e32 v143, v34
	ds_read_b64_tr_b16 v[170:171], v215 offset:0x1a00
	v_exp_f32_e32 v232, v35
	v_mfma_f32_32x32x16_bf16 v[96:111], a[204:207], a[172:175], v[96:111]
	v_cvt_pk_bf16_f32 v193, v146, v147
	ds_read_b64_tr_b16 v[160:161], v215 offset:0x1400
	v_exp_f32_e32 v233, v36
	v_exp_f32_e32 v234, v37
	v_mfma_f32_32x32x16_bf16 v[80:95], a[236:239], a[140:143], v[80:95]
	v_cvt_pk_bf16_f32 v194, v148, v149
	ds_read_b64_tr_b16 v[162:163], v215 offset:0x1c00
	ds_read_b64_tr_b16 v[136:137], v215 offset:0x1600
	v_exp_f32_e32 v239, v38
	v_exp_f32_e32 v240, v39
	v_mfma_f32_32x32x16_bf16 v[64:79], a[236:239], a[172:175], v[64:79]
	v_cvt_pk_bf16_f32 v195, v150, v151
	v_exp_f32_e32 v148, v40
	v_exp_f32_e32 v149, v41
	ds_read_b64_tr_b16 v[138:139], v215 offset:0x1e00
	v_mfma_f32_32x32x16_bf16 v[112:127], a[208:211], a[144:147], v[112:127]
	v_cvt_pk_bf16_f32 v144, v152, v153
	v_exp_f32_e32 v150, v42
	v_exp_f32_e32 v151, v43
	ds_read_b64_tr_b16 v[132:133], v215 offset:0x2000
	v_mfma_f32_32x32x16_bf16 v[96:111], a[208:211], a[176:179], v[96:111]
	v_cvt_pk_bf16_f32 v145, v154, v155
	v_exp_f32_e32 v152, v44
	v_exp_f32_e32 v153, v45
	ds_read_b64_tr_b16 v[134:135], v215 offset:0x2800
	v_mfma_f32_32x32x16_bf16 v[80:95], a[240:243], a[144:147], v[80:95]
	v_cvt_pk_bf16_f32 v146, v156, v157
	ds_read_b64_tr_b16 v[60:61], v215 offset:0x2200
	v_exp_f32_e32 v154, v46
	v_exp_f32_e32 v155, v47
	v_mfma_f32_32x32x16_bf16 v[64:79], a[240:243], a[176:179], v[64:79]
	ds_read_b64_tr_b16 v[62:63], v215 offset:0x2a00
	v_cvt_pk_bf16_f32 v147, v158, v159
	ds_read_b64_tr_b16 v[56:57], v215 offset:0x2400
	v_cvt_pk_bf16_f32 v52, v48, v49
	v_add_f32_e32 v32, v236, v48
	v_add_f32_e32 v33, v235, v49
	v_mfma_f32_32x32x16_bf16 v[112:127], a[212:215], a[148:151], v[112:127]
	s_add_i32 s12, s28, 0x80000
	s_mov_b32 s0, s12
	ds_read_b64_tr_b16 v[58:59], v215 offset:0x2c00
	v_cvt_pk_bf16_f32 v53, v50, v51
	v_add_f32_e32 v32, v32, v50
	v_add_f32_e32 v33, v33, v51
	ds_read_b64_tr_b16 v[48:49], v215 offset:0x2600
	v_mfma_f32_32x32x16_bf16 v[96:111], a[212:215], a[180:183], v[96:111]
	v_cvt_pk_bf16_f32 v54, v218, v219
	v_add_f32_e32 v32, v32, v218
	v_add_f32_e32 v33, v33, v219
	s_add_i32 s1, s28, 0x80400
	ds_read_b64_tr_b16 v[50:51], v215 offset:0x2e00
	ds_read_b64_tr_b16 v[44:45], v215 offset:0x3000
	v_mfma_f32_32x32x16_bf16 v[80:95], a[244:247], a[148:151], v[80:95]
	v_cvt_pk_bf16_f32 v55, v230, v231
	v_add_f32_e32 v32, v32, v230
	v_add_f32_e32 v33, v33, v231
	ds_read_b64_tr_b16 v[46:47], v215 offset:0x3800
	v_add_f32_e32 v32, v32, v220
	v_add_f32_e32 v33, v33, v221
	v_mfma_f32_32x32x16_bf16 v[64:79], a[244:247], a[180:183], v[64:79]
	s_add_i32 s13, s28, 0x80800
	s_mov_b32 s14, s13
	ds_read_b64_tr_b16 v[40:41], v215 offset:0x3200
	v_add_f32_e32 v32, v32, v222
	v_add_f32_e32 v33, v33, v223
	ds_read_b64_tr_b16 v[42:43], v215 offset:0x3a00
	v_add_f32_e32 v32, v32, v224
	v_mfma_f32_32x32x16_bf16 v[112:127], a[216:219], a[152:155], v[112:127]
	v_add_f32_e32 v33, v33, v227
	s_add_i32 s15, s28, 0x80c00
	ds_read_b64_tr_b16 v[36:37], v215 offset:0x3400
	ds_read_b64_tr_b16 v[38:39], v215 offset:0x3c00
	v_add_f32_e32 v156, v32, v228
	v_add_f32_e32 v157, v33, v229
	v_mfma_f32_32x32x16_bf16 v[96:111], a[216:219], a[184:187], v[96:111]
	ds_read_b64_tr_b16 v[32:33], v215 offset:0x3600
	v_cvt_pk_bf16_f32 v140, v141, v142
	v_add_f32_e32 v158, v237, v141
	v_add_f32_e32 v142, v238, v142
	s_add_i32 s27, s88, 0x0
	ds_read_b64_tr_b16 v[34:35], v215 offset:0x3e00
	v_mfma_f32_32x32x16_bf16 v[80:95], a[248:251], a[152:155], v[80:95]
	v_cvt_pk_bf16_f32 v141, v143, v232
	v_add_f32_e32 v143, v158, v143
	v_add_f32_e32 v158, v142, v232
	v_cvt_pk_bf16_f32 v142, v233, v234
	v_add_f32_e32 v159, v143, v233
	v_add_f32_e32 v158, v158, v234
	v_mfma_f32_32x32x16_bf16 v[64:79], a[248:251], a[184:187], v[64:79]
	s_add_i32 s30, s88, 0x80
	v_cvt_pk_bf16_f32 v143, v239, v240
	v_add_f32_e32 v159, v159, v239
	v_add_f32_e32 v158, v158, v240
	v_add_f32_e32 v159, v159, v148
	v_add_f32_e32 v158, v158, v149
	v_mfma_f32_32x32x16_bf16 v[112:127], a[220:223], a[156:159], v[112:127]
	s_add_i32 s31, s88, 0x800
	v_add_f32_e32 v159, v159, v150
	v_add_f32_e32 v158, v158, v151
	v_add_f32_e32 v159, v159, v152
	v_add_f32_e32 v158, v158, v153
	s_add_i32 s33, s88, 0x880
	v_add_f32_e32 v159, v159, v154
	v_mfma_f32_32x32x16_bf16 v[96:111], a[220:223], a[188:191], v[96:111]
	v_add_f32_e32 v158, v158, v155
	v_add_f32_e32 v156, v156, v157
	v_mfma_f32_32x32x16_bf16 v[80:95], a[252:255], a[156:159], v[80:95]
	v_mfma_f32_32x32x16_bf16 v[64:79], a[252:255], a[188:191], v[64:79]
	s_waitcnt vmcnt(0) lgkmcnt(0)
	s_barrier
	v_mfma_f32_32x32x16_bf16 a[0:15], v[180:183], v[164:167], a[0:15]
	v_mov_b32_e32 v157, v156
	v_mfma_f32_32x32x16_bf16 a[16:31], v[180:183], v[192:195], a[16:31]
	s_nop 1
	v_permlane32_swap_b32_e32 v156, v157
	v_add_f32_e32 v156, v156, v157
	ds_read_b128 a[192:195], v217 offset:0
	v_mfma_f32_32x32x16_bf16 a[32:47], v[188:191], v[164:167], a[32:47]
	v_add_f32_e32 v219, v225, v156
	v_add_f32_e32 v156, v159, v158
	v_mov_b32_e32 v157, v156
	ds_read_b128 a[196:199], v199 offset:0
	v_mfma_f32_32x32x16_bf16 a[48:63], v[188:191], v[192:195], a[48:63]
	v_permlane32_swap_b32_e32 v156, v157
	v_add_f32_e32 v156, v156, v157
	ds_read_b128 a[200:203], v198 offset:0
	s_mov_b32 m0, s23
	v_mfma_f32_32x32x16_bf16 a[64:79], v[176:179], v[164:167], a[64:79]
	v_add_f32_e32 v218, v226, v156
	buffer_load_dwordx4 v196, s[4:7], s27 offen lds
	ds_read_b128 a[204:207], v197 offset:0
	s_mov_b32 m0, s24
	v_mfma_f32_32x32x16_bf16 a[80:95], v[176:179], v[192:195], a[80:95]
	buffer_load_dwordx4 v196, s[4:7], s30 offen lds
	ds_read_b128 a[208:211], v217 offset:128
	s_mov_b32 m0, s25
	v_mfma_f32_32x32x16_bf16 a[96:111], v[184:187], v[164:167], a[96:111]
	buffer_load_dwordx4 v196, s[4:7], s31 offen lds
	ds_read_b128 a[212:215], v199 offset:128
	s_mov_b32 m0, s26
	v_mfma_f32_32x32x16_bf16 a[112:127], v[184:187], v[192:195], a[112:127]
	buffer_load_dwordx4 v196, s[4:7], s33 offen lds
	ds_read_b128 a[216:219], v198 offset:128
	v_mfma_f32_32x32x16_bf16 a[0:15], v[172:175], v[128:131], a[0:15]
	ds_read_b128 a[220:223], v197 offset:128
	v_max3_f32 v156, v112, v113, v80
	v_max3_f32 v157, v114, v115, v81
	v_max3_f32 v156, v156, v82, v83
	v_mfma_f32_32x32x16_bf16 a[16:31], v[172:175], v[144:147], a[16:31]
	ds_read_b128 a[224:227], v217 offset:8192
	v_max3_f32 v156, v156, v116, v117
	v_max3_f32 v157, v157, v118, v119
	v_max3_f32 v156, v156, v84, v85
	v_max3_f32 v157, v157, v86, v87
	v_mfma_f32_32x32x16_bf16 a[32:47], v[168:171], v[128:131], a[32:47]
	ds_read_b128 a[228:231], v199 offset:8192
	v_max3_f32 v156, v156, v120, v121
	v_max3_f32 v157, v157, v122, v123
	v_max3_f32 v156, v156, v88, v89
	v_max3_f32 v157, v157, v90, v91
	v_mfma_f32_32x32x16_bf16 a[48:63], v[168:171], v[144:147], a[48:63]
	ds_read_b128 a[232:235], v198 offset:8192
	v_max3_f32 v156, v156, v124, v125
	v_max3_f32 v157, v157, v126, v127
	v_max3_f32 v156, v156, v92, v93
	v_max3_f32 v157, v157, v94, v95
	v_mfma_f32_32x32x16_bf16 a[64:79], v[160:163], v[128:131], a[64:79]
	ds_read_b128 a[236:239], v197 offset:8192
	v_max3_f32 v158, v96, v97, v64
	v_max3_f32 v159, v98, v99, v65
	v_max3_f32 v158, v158, v66, v67
	v_mfma_f32_32x32x16_bf16 a[80:95], v[160:163], v[144:147], a[80:95]
	ds_read_b128 a[240:243], v217 offset:8320
	v_max3_f32 v158, v158, v100, v101
	v_max3_f32 v159, v159, v102, v103
	v_max3_f32 v158, v158, v68, v69
	v_max3_f32 v159, v159, v70, v71
	v_mfma_f32_32x32x16_bf16 a[96:111], v[136:139], v[128:131], a[96:111]
	ds_read_b128 a[244:247], v199 offset:8320
	v_max3_f32 v128, v158, v104, v105
	v_max3_f32 v129, v159, v106, v107
	v_max3_f32 v128, v128, v72, v73
	v_max3_f32 v129, v129, v74, v75
	v_mfma_f32_32x32x16_bf16 a[112:127], v[136:139], v[144:147], a[112:127]
	ds_read_b128 a[248:251], v198 offset:8320
	v_max3_f32 v128, v128, v108, v109
	v_max3_f32 v129, v129, v110, v111
	v_max3_f32 v128, v128, v76, v77
	v_max3_f32 v130, v129, v78, v79
	v_mfma_f32_32x32x16_bf16 a[0:15], v[132:135], v[52:55], a[0:15]
	ds_read_b128 a[252:255], v197 offset:8320
	v_max_f32_e32 v129, v156, v157
	v_mov_b32_e32 v131, v129
	s_nop 1
	v_permlane32_swap_b32_e32 v129, v131
	v_max_f32_e32 v129, v129, v131
	v_mfma_f32_32x32x16_bf16 a[16:31], v[132:135], v[140:143], a[16:31]
	v_max_f32_e32 v128, v128, v130
	v_mov_b32_e32 v130, v128
	s_nop 1
	v_permlane32_swap_b32_e32 v128, v130
	v_max_f32_e32 v128, v128, v130
	v_max_f32_e32 v130, v129, v129
	v_max_f32_e32 v131, v128, v128
	v_max_f32_e32 v130, v130, v131
	s_mov_b32 s0, 0x41000000
	v_mfma_f32_32x32x16_bf16 a[32:47], v[60:63], v[52:55], a[32:47]
	v_cmp_lt_f32_e32 vcc, s0, v130
	s_cmp_lg_u64 vcc, 0
	s_cselect_b64 s[0:1], -1, 0
	s_cbranch_vccnz .LBB0_43
.LBB0_37:
	v_mfma_f32_32x32x16_bf16 a[48:63], v[60:63], v[140:143], a[48:63]
	v_cvt_pk_bf16_f32 v156, v220, v221
	v_cvt_pk_bf16_f32 v157, v222, v223
	v_cvt_pk_bf16_f32 v158, v224, v227
	v_cvt_pk_bf16_f32 v159, v228, v229
	v_cvt_pk_bf16_f32 v160, v148, v149
	v_cvt_pk_bf16_f32 v161, v150, v151
	v_cvt_pk_bf16_f32 v162, v152, v153
	v_cvt_pk_bf16_f32 v163, v154, v155
	v_mfma_f32_32x32x16_bf16 a[64:79], v[56:59], v[52:55], a[64:79]
	v_exp_f32_e32 v128, v112
	v_exp_f32_e32 v129, v113
	v_exp_f32_e32 v130, v114
	v_exp_f32_e32 v131, v115
	v_mfma_f32_32x32x16_bf16 a[80:95], v[56:59], v[140:143], a[80:95]
	v_mov_b32_e32 v60, 0
	v_add_f32_e32 v61, v60, v128
	v_add_f32_e32 v62, v60, v129
	v_exp_f32_e32 v132, v116
	v_exp_f32_e32 v133, v117
	v_exp_f32_e32 v134, v118
	v_mfma_f32_32x32x16_bf16 a[96:111], v[48:51], v[52:55], a[96:111]
	v_add_f32_e32 v56, v61, v130
	v_add_f32_e32 v57, v62, v131
	v_exp_f32_e32 v135, v119
	v_exp_f32_e32 v136, v120
	v_add_f32_e32 v52, v56, v132
	v_add_f32_e32 v53, v57, v133
	v_mfma_f32_32x32x16_bf16 a[112:127], v[48:51], v[140:143], a[112:127]
	v_add_f32_e32 v52, v52, v134
	v_exp_f32_e32 v137, v121
	v_exp_f32_e32 v138, v122
	v_exp_f32_e32 v139, v123
	v_add_f32_e32 v48, v53, v135
	v_mfma_f32_32x32x16_bf16 a[0:15], v[44:47], v[156:159], a[0:15]
	v_add_f32_e32 v49, v52, v136
	v_exp_f32_e32 v140, v124
	v_exp_f32_e32 v141, v125
	v_add_f32_e32 v48, v48, v137
	v_add_f32_e32 v49, v49, v138
	v_add_f32_e32 v48, v48, v139
	v_mfma_f32_32x32x16_bf16 a[16:31], v[44:47], v[160:163], a[16:31]
	v_exp_f32_e32 v142, v126
	v_exp_f32_e32 v143, v127
	v_exp_f32_e32 v144, v96
	v_add_f32_e32 v44, v49, v140
	v_add_f32_e32 v45, v48, v141
	v_mfma_f32_32x32x16_bf16 a[32:47], v[40:43], v[156:159], a[32:47]
	v_exp_f32_e32 v145, v97
	v_exp_f32_e32 v146, v98
	v_add_f32_e32 v226, v44, v142
	v_add_f32_e32 v224, v45, v143
	v_add_f32_e32 v44, v60, v144
	v_exp_f32_e32 v147, v99
	v_mfma_f32_32x32x16_bf16 a[48:63], v[40:43], v[160:163], a[48:63]
	v_exp_f32_e32 v148, v100
	v_exp_f32_e32 v149, v101
	v_add_f32_e32 v40, v60, v145
	v_add_f32_e32 v41, v44, v146
	v_exp_f32_e32 v150, v102
	v_mfma_f32_32x32x16_bf16 a[64:79], v[36:39], v[156:159], a[64:79]
	v_exp_f32_e32 v151, v103
	v_add_f32_e32 v40, v40, v147
	v_add_f32_e32 v41, v41, v148
	v_add_f32_e32 v40, v40, v149
	v_exp_f32_e32 v152, v104
	v_exp_f32_e32 v153, v105
	v_mfma_f32_32x32x16_bf16 a[80:95], v[36:39], v[160:163], a[80:95]
	v_exp_f32_e32 v154, v106
	v_add_f32_e32 v36, v41, v150
	v_add_f32_e32 v37, v40, v151
	v_exp_f32_e32 v155, v107
	v_add_f32_e32 v36, v36, v152
	v_add_f32_e32 v37, v37, v153
	v_mfma_f32_32x32x16_bf16 a[96:111], v[32:35], v[156:159], a[96:111]
	v_exp_f32_e32 v156, v108
	v_add_f32_e32 v36, v36, v154
	v_exp_f32_e32 v157, v109
	v_exp_f32_e32 v158, v110
	v_exp_f32_e32 v159, v111
	v_mfma_f32_32x32x16_bf16 a[112:127], v[32:35], v[160:163], a[112:127]
	v_add_f32_e32 v32, v37, v155
	v_add_f32_e32 v33, v36, v156
	s_andn2_b64 vcc, exec, s[0:1]
	v_add_f32_e32 v32, v32, v157
	v_add_f32_e32 v223, v33, v158
	s_nop 0
	v_add_f32_e32 v225, v32, v159
	s_cbranch_vccz .LBB0_44
.LBB0_38:
	s_waitcnt lgkmcnt(0)
	v_mfma_f32_32x32x16_bf16 v[112:127], a[192:195], a[128:131], v[0:15]
	ds_read_b64_tr_b16 v[172:173], v212 offset:0
	v_exp_f32_e32 v227, v80
	v_exp_f32_e32 v228, v81
	v_mfma_f32_32x32x16_bf16 v[96:111], a[192:195], a[160:163], v[16:31]
	v_cvt_pk_bf16_f32 v164, v128, v129
	v_exp_f32_e32 v82, v82
	v_exp_f32_e32 v83, v83
	v_mfma_f32_32x32x16_bf16 v[48:63], a[224:227], a[128:131], v[0:15]
	ds_read_b64_tr_b16 v[174:175], v212 offset:0x800
	v_cvt_pk_bf16_f32 v165, v130, v131
	v_exp_f32_e32 v84, v84
	v_exp_f32_e32 v85, v85
	v_mfma_f32_32x32x16_bf16 v[32:47], a[224:227], a[160:163], v[16:31]
	ds_read_b64_tr_b16 v[180:181], v212 offset:0x200
	v_cvt_pk_bf16_f32 v166, v132, v133
	ds_read_b64_tr_b16 v[182:183], v212 offset:0xa00
	v_exp_f32_e32 v86, v86
	v_mfma_f32_32x32x16_bf16 v[112:127], a[196:199], a[132:135], v[112:127]
	v_exp_f32_e32 v87, v87
	ds_read_b64_tr_b16 v[184:185], v212 offset:0x400
	v_cvt_pk_bf16_f32 v167, v134, v135
	v_exp_f32_e32 v80, v88
	v_mfma_f32_32x32x16_bf16 v[96:111], a[196:199], a[164:167], v[96:111]
	v_exp_f32_e32 v81, v89
	ds_read_b64_tr_b16 v[186:187], v212 offset:0xc00
	v_cvt_pk_bf16_f32 v160, v136, v137
	v_exp_f32_e32 v90, v90
	v_mfma_f32_32x32x16_bf16 v[48:63], a[228:231], a[132:135], v[48:63]
	v_exp_f32_e32 v91, v91
	ds_read_b64_tr_b16 v[192:193], v212 offset:0x600
	v_cvt_pk_bf16_f32 v161, v138, v139
	v_exp_f32_e32 v217, v92
	v_mfma_f32_32x32x16_bf16 v[32:47], a[228:231], a[164:167], v[32:47]
	v_exp_f32_e32 v220, v93
	ds_read_b64_tr_b16 v[194:195], v212 offset:0xe00
	v_cvt_pk_bf16_f32 v162, v140, v141
	ds_read_b64_tr_b16 v[188:189], v212 offset:0x1000
	v_mfma_f32_32x32x16_bf16 v[112:127], a[200:203], a[136:139], v[112:127]
	v_exp_f32_e32 v221, v94
	v_exp_f32_e32 v222, v95
	ds_read_b64_tr_b16 v[190:191], v212 offset:0x1800
	v_mfma_f32_32x32x16_bf16 v[96:111], a[200:203], a[168:171], v[96:111]
	v_cvt_pk_bf16_f32 v163, v142, v143
	v_exp_f32_e32 v130, v64
	v_exp_f32_e32 v131, v65
	v_mfma_f32_32x32x16_bf16 v[48:63], a[232:235], a[136:139], v[48:63]
	ds_read_b64_tr_b16 v[176:177], v212 offset:0x1200
	v_cvt_pk_bf16_f32 v196, v144, v145
	v_exp_f32_e32 v138, v66
	v_exp_f32_e32 v139, v67
	v_mfma_f32_32x32x16_bf16 v[32:47], a[232:235], a[168:171], v[32:47]
	ds_read_b64_tr_b16 v[178:179], v212 offset:0x1a00
	v_cvt_pk_bf16_f32 v197, v146, v147
	ds_read_b64_tr_b16 v[168:169], v212 offset:0x1400
	v_exp_f32_e32 v229, v68
	v_mfma_f32_32x32x16_bf16 v[112:127], a[204:207], a[140:143], v[112:127]
	v_exp_f32_e32 v230, v69
	v_cvt_pk_bf16_f32 v198, v148, v149
	ds_read_b64_tr_b16 v[170:171], v212 offset:0x1c00
	ds_read_b64_tr_b16 v[144:145], v212 offset:0x1600
	v_mfma_f32_32x32x16_bf16 v[96:111], a[204:207], a[172:175], v[96:111]
	v_exp_f32_e32 v231, v70
	v_exp_f32_e32 v232, v71
	v_cvt_pk_bf16_f32 v199, v150, v151
	v_mfma_f32_32x32x16_bf16 v[48:63], a[236:239], a[140:143], v[48:63]
	v_exp_f32_e32 v64, v72
	v_exp_f32_e32 v65, v73
	ds_read_b64_tr_b16 v[146:147], v212 offset:0x1e00
	v_mfma_f32_32x32x16_bf16 v[32:47], a[236:239], a[172:175], v[32:47]
	v_cvt_pk_bf16_f32 v148, v152, v153
	v_exp_f32_e32 v70, v74
	v_exp_f32_e32 v71, v75
	v_mfma_f32_32x32x16_bf16 v[112:127], a[208:211], a[144:147], v[112:127]
	ds_read_b64_tr_b16 v[140:141], v212 offset:0x2000
	v_cvt_pk_bf16_f32 v149, v154, v155
	v_exp_f32_e32 v154, v76
	v_exp_f32_e32 v155, v77
	v_mfma_f32_32x32x16_bf16 v[96:111], a[208:211], a[176:179], v[96:111]
	ds_read_b64_tr_b16 v[142:143], v212 offset:0x2800
	v_cvt_pk_bf16_f32 v150, v156, v157
	ds_read_b64_tr_b16 v[66:67], v212 offset:0x2200
	v_exp_f32_e32 v156, v78
	v_mfma_f32_32x32x16_bf16 v[48:63], a[240:243], a[144:147], v[48:63]
	v_exp_f32_e32 v157, v79
	ds_read_b64_tr_b16 v[68:69], v212 offset:0x2a00
	v_cvt_pk_bf16_f32 v151, v158, v159
	ds_read_b64_tr_b16 v[132:133], v212 offset:0x2400
	v_mfma_f32_32x32x16_bf16 v[32:47], a[240:243], a[176:179], v[32:47]
	v_cvt_pk_bf16_f32 v72, v227, v228
	v_add_f32_e32 v74, v226, v227
	v_add_f32_e32 v75, v224, v228
	s_add_i32 s0, s28, 0x84000
	ds_read_b64_tr_b16 v[134:135], v212 offset:0x2c00
	v_cvt_pk_bf16_f32 v73, v82, v83
	v_mfma_f32_32x32x16_bf16 v[112:127], a[212:215], a[148:151], v[112:127]
	v_add_f32_e32 v78, v74, v82
	v_add_f32_e32 v75, v75, v83
	ds_read_b64_tr_b16 v[76:77], v212 offset:0x2600
	v_cvt_pk_bf16_f32 v74, v84, v85
	v_add_f32_e32 v84, v78, v84
	v_mfma_f32_32x32x16_bf16 v[96:111], a[212:215], a[180:183], v[96:111]
	v_add_f32_e32 v85, v75, v85
	s_add_i32 s1, s28, 0x84400
	ds_read_b64_tr_b16 v[78:79], v212 offset:0x2e00
	ds_read_b64_tr_b16 v[82:83], v212 offset:0x3000
	v_cvt_pk_bf16_f32 v75, v86, v87
	v_add_f32_e32 v86, v84, v86
	v_mfma_f32_32x32x16_bf16 v[48:63], a[244:247], a[148:151], v[48:63]
	v_add_f32_e32 v87, v85, v87
	ds_read_b64_tr_b16 v[84:85], v212 offset:0x3800
	v_add_f32_e32 v88, v86, v80
	v_add_f32_e32 v89, v87, v81
	s_add_i32 s4, s28, 0x84800
	ds_read_b64_tr_b16 v[86:87], v212 offset:0x3200
	v_mfma_f32_32x32x16_bf16 v[32:47], a[244:247], a[180:183], v[32:47]
	v_add_f32_e32 v92, v88, v90
	v_add_f32_e32 v93, v89, v91
	ds_read_b64_tr_b16 v[88:89], v212 offset:0x3a00
	v_add_f32_e32 v128, v92, v217
	v_add_f32_e32 v129, v93, v220
	v_mfma_f32_32x32x16_bf16 v[112:127], a[216:219], a[152:155], v[112:127]
	s_add_i32 s5, s28, 0x84c00
	ds_read_b64_tr_b16 v[92:93], v212 offset:0x3400
	ds_read_b64_tr_b16 v[94:95], v212 offset:0x3c00
	v_add_f32_e32 v152, v128, v221
	v_add_f32_e32 v153, v129, v222
	ds_read_b64_tr_b16 v[128:129], v212 offset:0x3600
	v_mfma_f32_32x32x16_bf16 v[96:111], a[216:219], a[184:187], v[96:111]
	v_cvt_pk_bf16_f32 v136, v130, v131
	v_add_f32_e32 v158, v223, v130
	v_add_f32_e32 v159, v225, v131
	ds_read_b64_tr_b16 v[130:131], v212 offset:0x3e00
	v_cvt_pk_bf16_f32 v137, v138, v139
	v_mfma_f32_32x32x16_bf16 v[48:63], a[248:251], a[152:155], v[48:63]
	v_add_f32_e32 v158, v158, v138
	v_add_f32_e32 v139, v159, v139
	v_cvt_pk_bf16_f32 v138, v229, v230
	v_add_f32_e32 v158, v158, v229
	v_add_f32_e32 v159, v139, v230
	v_mfma_f32_32x32x16_bf16 v[32:47], a[248:251], a[184:187], v[32:47]
	s_add_i32 s6, s28, 0x80080
	v_cvt_pk_bf16_f32 v139, v231, v232
	v_add_f32_e32 v158, v158, v231
	v_add_f32_e32 v159, v159, v232
	v_add_f32_e32 v158, v158, v64
	v_add_f32_e32 v159, v159, v65
	v_mfma_f32_32x32x16_bf16 v[112:127], a[220:223], a[156:159], v[112:127]
	v_add_f32_e32 v158, v158, v70
	v_add_f32_e32 v159, v159, v71
	v_add_f32_e32 v158, v158, v154
	v_add_f32_e32 v159, v159, v155
	s_add_i32 s7, s28, 0x80880
	v_add_f32_e32 v158, v158, v156
	v_mfma_f32_32x32x16_bf16 v[96:111], a[220:223], a[188:191], v[96:111]
	v_add_f32_e32 v159, v159, v157
	v_add_f32_e32 v152, v152, v153
	v_mfma_f32_32x32x16_bf16 v[48:63], a[252:255], a[156:159], v[48:63]
	v_mfma_f32_32x32x16_bf16 v[32:47], a[252:255], a[188:191], v[32:47]
	s_waitcnt vmcnt(0) lgkmcnt(0)
	s_barrier
	v_mfma_f32_32x32x16_bf16 a[0:15], v[172:175], v[164:167], a[0:15]
	v_mov_b32_e32 v153, v152
	v_mfma_f32_32x32x16_bf16 a[16:31], v[172:175], v[196:199], a[16:31]
	s_nop 1
	v_permlane32_swap_b32_e32 v152, v153
	v_add_f32_e32 v152, v152, v153
	v_mfma_f32_32x32x16_bf16 a[32:47], v[180:183], v[164:167], a[32:47]
	v_add_f32_e32 v153, v219, v152
	v_add_f32_e32 v152, v158, v159
	v_mov_b32_e32 v158, v152
	v_mfma_f32_32x32x16_bf16 a[48:63], v[180:183], v[196:199], a[48:63]
	s_nop 1
	v_permlane32_swap_b32_e32 v152, v158
	v_add_f32_e32 v152, v152, v158
	v_mfma_f32_32x32x16_bf16 a[64:79], v[184:187], v[164:167], a[64:79]
	v_add_f32_e32 v152, v218, v152
	v_mfma_f32_32x32x16_bf16 a[80:95], v[184:187], v[196:199], a[80:95]
	v_mfma_f32_32x32x16_bf16 a[96:111], v[192:195], v[164:167], a[96:111]
	v_mfma_f32_32x32x16_bf16 a[112:127], v[192:195], v[196:199], a[112:127]
	v_mfma_f32_32x32x16_bf16 a[0:15], v[188:191], v[160:163], a[0:15]
	v_max3_f32 v158, v112, v113, v48
	v_max3_f32 v159, v114, v115, v49
	v_max3_f32 v158, v158, v50, v51
	v_mfma_f32_32x32x16_bf16 a[16:31], v[188:191], v[148:151], a[16:31]
	v_max3_f32 v158, v158, v116, v117
	v_max3_f32 v159, v159, v118, v119
	v_max3_f32 v158, v158, v52, v53
	v_max3_f32 v159, v159, v54, v55
	v_mfma_f32_32x32x16_bf16 a[32:47], v[176:179], v[160:163], a[32:47]
	v_max3_f32 v158, v158, v120, v121
	v_max3_f32 v159, v159, v122, v123
	v_max3_f32 v158, v158, v56, v57
	v_max3_f32 v159, v159, v58, v59
	v_mfma_f32_32x32x16_bf16 a[48:63], v[176:179], v[148:151], a[48:63]
	v_max3_f32 v158, v158, v124, v125
	v_max3_f32 v159, v159, v126, v127
	v_max3_f32 v158, v158, v60, v61
	v_max3_f32 v159, v159, v62, v63
	v_mfma_f32_32x32x16_bf16 a[64:79], v[168:171], v[160:163], a[64:79]
	v_max3_f32 v164, v96, v97, v32
	v_max3_f32 v165, v98, v99, v33
	v_max3_f32 v164, v164, v34, v35
	v_mfma_f32_32x32x16_bf16 a[80:95], v[168:171], v[148:151], a[80:95]
	v_max3_f32 v164, v164, v100, v101
	v_max3_f32 v165, v165, v102, v103
	v_max3_f32 v164, v164, v36, v37
	v_max3_f32 v165, v165, v38, v39
	v_mfma_f32_32x32x16_bf16 a[96:111], v[144:147], v[160:163], a[96:111]
	v_max3_f32 v160, v164, v104, v105
	v_max3_f32 v161, v165, v106, v107
	v_max3_f32 v160, v160, v40, v41
	v_max3_f32 v161, v161, v42, v43
	v_mfma_f32_32x32x16_bf16 a[112:127], v[144:147], v[148:151], a[112:127]
	v_max3_f32 v145, v161, v110, v111
	v_max3_f32 v144, v160, v108, v109
	v_max3_f32 v146, v144, v44, v45
	v_max3_f32 v145, v145, v46, v47
	v_mfma_f32_32x32x16_bf16 a[0:15], v[140:143], v[72:75], a[0:15]
	v_max_f32_e32 v144, v158, v159
	v_mov_b32_e32 v147, v144
	s_nop 1
	v_permlane32_swap_b32_e32 v144, v147
	v_max_f32_e32 v144, v144, v147
	v_mfma_f32_32x32x16_bf16 a[16:31], v[140:143], v[136:139], a[16:31]
	v_max_f32_e32 v140, v146, v145
	v_mov_b32_e32 v141, v140
	s_nop 1
	v_permlane32_swap_b32_e32 v140, v141
	v_max_f32_e32 v140, v140, v141
	v_max_f32_e32 v141, v144, v144
	v_max_f32_e32 v142, v140, v140
	v_max_f32_e32 v141, v141, v142
	s_mov_b32 s0, 0x41000000
	v_mfma_f32_32x32x16_bf16 a[32:47], v[66:69], v[72:75], a[32:47]
	v_cmp_lt_f32_e32 vcc, s0, v141
	s_cmp_lg_u64 vcc, 0
	s_cselect_b64 s[0:1], -1, 0
	s_cbranch_vccnz .LBB0_45
.LBB0_39:
	v_mfma_f32_32x32x16_bf16 a[48:63], v[66:69], v[136:139], a[48:63]
	v_cvt_pk_bf16_f32 v140, v80, v81
	v_cvt_pk_bf16_f32 v141, v90, v91
	v_cvt_pk_bf16_f32 v142, v217, v220
	v_cvt_pk_bf16_f32 v143, v221, v222
	v_cvt_pk_bf16_f32 v144, v64, v65
	v_cvt_pk_bf16_f32 v145, v70, v71
	v_cvt_pk_bf16_f32 v146, v154, v155
	v_cvt_pk_bf16_f32 v147, v156, v157
	v_mfma_f32_32x32x16_bf16 a[64:79], v[132:135], v[72:75], a[64:79]
	v_exp_f32_e32 v64, v112
	v_exp_f32_e32 v65, v113
	v_exp_f32_e32 v66, v114
	v_exp_f32_e32 v67, v115
	v_mfma_f32_32x32x16_bf16 a[80:95], v[132:135], v[136:139], a[80:95]
	v_mov_b32_e32 v90, 0
	v_add_f32_e32 v71, v90, v64
	v_add_f32_e32 v80, v90, v65
	v_exp_f32_e32 v68, v116
	v_exp_f32_e32 v69, v117
	v_exp_f32_e32 v70, v118
	v_mfma_f32_32x32x16_bf16 a[96:111], v[76:79], v[72:75], a[96:111]
	v_add_f32_e32 v81, v71, v66
	v_add_f32_e32 v80, v80, v67
	v_exp_f32_e32 v71, v119
	v_exp_f32_e32 v72, v120
	v_add_f32_e32 v73, v81, v68
	v_add_f32_e32 v80, v80, v69
	v_mfma_f32_32x32x16_bf16 a[112:127], v[76:79], v[136:139], a[112:127]
	v_add_f32_e32 v81, v73, v70
	v_exp_f32_e32 v73, v121
	v_exp_f32_e32 v74, v122
	v_exp_f32_e32 v75, v123
	v_add_f32_e32 v78, v80, v71
	v_mfma_f32_32x32x16_bf16 a[0:15], v[82:85], v[140:143], a[0:15]
	v_add_f32_e32 v79, v81, v72
	v_exp_f32_e32 v76, v124
	v_exp_f32_e32 v77, v125
	v_add_f32_e32 v78, v78, v73
	v_add_f32_e32 v81, v79, v74
	v_add_f32_e32 v91, v78, v75
	v_mfma_f32_32x32x16_bf16 a[16:31], v[82:85], v[144:147], a[16:31]
	v_exp_f32_e32 v78, v126
	v_exp_f32_e32 v79, v127
	v_exp_f32_e32 v80, v96
	v_add_f32_e32 v83, v81, v76
	v_add_f32_e32 v84, v91, v77
	v_mfma_f32_32x32x16_bf16 a[32:47], v[86:89], v[140:143], a[32:47]
	v_exp_f32_e32 v81, v97
	v_exp_f32_e32 v82, v98
	v_add_f32_e32 v133, v83, v78
	v_add_f32_e32 v132, v84, v79
	v_add_f32_e32 v91, v90, v80
	v_exp_f32_e32 v83, v99
	v_mfma_f32_32x32x16_bf16 a[48:63], v[86:89], v[144:147], a[48:63]
	v_exp_f32_e32 v84, v100
	v_exp_f32_e32 v85, v101
	v_add_f32_e32 v88, v90, v81
	v_add_f32_e32 v89, v91, v82
	v_exp_f32_e32 v86, v102
	v_mfma_f32_32x32x16_bf16 a[64:79], v[92:95], v[140:143], a[64:79]
	v_exp_f32_e32 v87, v103
	v_add_f32_e32 v88, v88, v83
	v_add_f32_e32 v91, v89, v84
	v_add_f32_e32 v96, v88, v85
	v_exp_f32_e32 v88, v104
	v_exp_f32_e32 v89, v105
	v_mfma_f32_32x32x16_bf16 a[80:95], v[92:95], v[144:147], a[80:95]
	v_exp_f32_e32 v90, v106
	v_add_f32_e32 v93, v91, v86
	v_add_f32_e32 v94, v96, v87
	v_exp_f32_e32 v91, v107
	v_exp_f32_e32 v92, v108
	v_mfma_f32_32x32x16_bf16 a[96:111], v[128:131], v[140:143], a[96:111]
	v_add_f32_e32 v93, v93, v88
	v_add_f32_e32 v96, v94, v89
	v_add_f32_e32 v97, v93, v90
	v_exp_f32_e32 v93, v109
	v_exp_f32_e32 v94, v110
	v_exp_f32_e32 v95, v111
	v_mfma_f32_32x32x16_bf16 a[112:127], v[128:131], v[144:147], a[112:127]
	v_add_f32_e32 v96, v96, v91
	v_add_f32_e32 v97, v97, v92
	s_andn2_b64 vcc, exec, s[0:1]
	v_add_f32_e32 v0, v96, v93
	v_add_f32_e32 v129, v97, v94
	s_nop 0
	v_add_f32_e32 v130, v0, v95
	s_cbranch_vccz .LBB0_46
